# instruction-fetch alignment: MLA step, SB tile and the eight GEMM K-loop heads pinned to 64-byte boundaries (s_nop fill)
# speedup vs baseline: 1.0066x; 1.0066x over previous
; template <class P, bool ALIGN_EPI>
; __device__ __forceinline__ void gemm_phase(ldsp lds, ldsp tab, const P& S) {
;     ...
;             for (int t = 0; t < nt; t += 2) PG8_TRIP(t, PG8_MMA);
;     ...
;         if constexpr (!P::FP8) {
; #pragma unroll
;             for (int a = 0; a < 2; ++a)
; #pragma unroll
;                 for (int b = 0; b < 2; ++b)
; #pragma unroll
;                     for (int m = 0; m < 4; ++m)
; #pragma unroll
;                         for (int n = 0; n < 2; ++n) acc[a][b][m][n] = (f32x4){0.f, 0.f, 0.f, 0.f}; }
;         cur = nxt; cA = nA; cB = nB; ++ui;
.LBB0_846:
	s_ashr_i32 s17, s16, 31
	s_lshl_b64 s[18:19], s[16:17], 19
	s_add_u32 s18, s50, s18
	s_addc_u32 s19, s51, s19
	s_ashr_i32 s15, s14, 31
	s_lshl_b64 s[20:21], s[14:15], 19
	s_add_u32 s20, s52, s20
	v_mov_b32_e32 v4, 0
	s_addc_u32 s21, s53, s21
	s_mov_b32 s3, -2
	s_mov_b64 s[38:39], 0x40080
	v_mov_b32_e32 v5, v4
	v_mov_b32_e32 v6, v4
	v_mov_b32_e32 v7, v4
	v_mov_b32_e32 v8, v4
	v_mov_b32_e32 v9, v4
	v_mov_b32_e32 v10, v4
	v_mov_b32_e32 v11, v4
	v_mov_b32_e32 v20, v4
	v_mov_b32_e32 v21, v4
	v_mov_b32_e32 v22, v4
	v_mov_b32_e32 v23, v4
	v_mov_b32_e32 v24, v4
	v_mov_b32_e32 v25, v4
	v_mov_b32_e32 v26, v4
	v_mov_b32_e32 v27, v4
	v_mov_b32_e32 v36, v4
	v_mov_b32_e32 v37, v4
	v_mov_b32_e32 v38, v4
	v_mov_b32_e32 v39, v4
	v_mov_b32_e32 v40, v4
	v_mov_b32_e32 v41, v4
	v_mov_b32_e32 v42, v4
	v_mov_b32_e32 v43, v4
	v_mov_b32_e32 v52, v4
	v_mov_b32_e32 v53, v4
	v_mov_b32_e32 v54, v4
	v_mov_b32_e32 v55, v4
	v_mov_b32_e32 v56, v4
	v_mov_b32_e32 v57, v4
	v_mov_b32_e32 v58, v4
	v_mov_b32_e32 v59, v4
	v_mov_b32_e32 v12, v4
	v_mov_b32_e32 v13, v4
	v_mov_b32_e32 v14, v4
	v_mov_b32_e32 v15, v4
	v_mov_b32_e32 v16, v4
	v_mov_b32_e32 v17, v4
	v_mov_b32_e32 v18, v4
	v_mov_b32_e32 v19, v4
	v_mov_b32_e32 v28, v4
	v_mov_b32_e32 v29, v4
	v_mov_b32_e32 v30, v4
	v_mov_b32_e32 v31, v4
	v_mov_b32_e32 v32, v4
	v_mov_b32_e32 v33, v4
	v_mov_b32_e32 v34, v4
	v_mov_b32_e32 v35, v4
	v_mov_b32_e32 v44, v4
	v_mov_b32_e32 v45, v4
	v_mov_b32_e32 v46, v4
	v_mov_b32_e32 v47, v4
	v_mov_b32_e32 v48, v4
	v_mov_b32_e32 v49, v4
	v_mov_b32_e32 v50, v4
	v_mov_b32_e32 v51, v4
	v_mov_b32_e32 v60, v4
	v_mov_b32_e32 v61, v4
	v_mov_b32_e32 v62, v4
	v_mov_b32_e32 v63, v4
	v_mov_b32_e32 v64, v4
	v_mov_b32_e32 v65, v4
	v_mov_b32_e32 v66, v4
	v_mov_b32_e32 v67, v4
	v_mov_b32_e32 v80, v4
	v_mov_b32_e32 v81, v4
	v_mov_b32_e32 v82, v4
	v_mov_b32_e32 v83, v4
	v_mov_b32_e32 v88, v4
	v_mov_b32_e32 v89, v4
	v_mov_b32_e32 v90, v4
	v_mov_b32_e32 v91, v4
	v_mov_b32_e32 v108, v4
	v_mov_b32_e32 v109, v4
	v_mov_b32_e32 v110, v4
	v_mov_b32_e32 v111, v4
	v_mov_b32_e32 v112, v4
	v_mov_b32_e32 v113, v4
	v_mov_b32_e32 v114, v4
	v_mov_b32_e32 v115, v4
	v_mov_b32_e32 v132, v4
	v_mov_b32_e32 v133, v4
	v_mov_b32_e32 v134, v4
	v_mov_b32_e32 v135, v4
	v_mov_b32_e32 v136, v4
	v_mov_b32_e32 v137, v4
	v_mov_b32_e32 v138, v4
	v_mov_b32_e32 v139, v4
	v_mov_b32_e32 v156, v4
	v_mov_b32_e32 v157, v4
	v_mov_b32_e32 v158, v4
	v_mov_b32_e32 v159, v4
	v_mov_b32_e32 v160, v4
	v_mov_b32_e32 v161, v4
	v_mov_b32_e32 v162, v4
	v_mov_b32_e32 v163, v4
	v_mov_b32_e32 v96, v4
	v_mov_b32_e32 v97, v4
	v_mov_b32_e32 v98, v4
	v_mov_b32_e32 v99, v4
	v_mov_b32_e32 v104, v4
	v_mov_b32_e32 v105, v4
	v_mov_b32_e32 v106, v4
	v_mov_b32_e32 v107, v4
	v_mov_b32_e32 v120, v4
	v_mov_b32_e32 v121, v4
	v_mov_b32_e32 v122, v4
	v_mov_b32_e32 v123, v4
	v_mov_b32_e32 v124, v4
	v_mov_b32_e32 v125, v4
	v_mov_b32_e32 v126, v4
	v_mov_b32_e32 v127, v4
	v_mov_b32_e32 v144, v4
	v_mov_b32_e32 v145, v4
	v_mov_b32_e32 v146, v4
	v_mov_b32_e32 v147, v4
	v_mov_b32_e32 v148, v4
	v_mov_b32_e32 v149, v4
	v_mov_b32_e32 v150, v4
	v_mov_b32_e32 v151, v4
	v_mov_b32_e32 v168, v4
	v_mov_b32_e32 v169, v4
	v_mov_b32_e32 v170, v4
	v_mov_b32_e32 v171, v4
	v_mov_b32_e32 v176, v4
	v_mov_b32_e32 v177, v4
	v_mov_b32_e32 v178, v4
	v_mov_b32_e32 v179, v4
	.p2alignl 6, 3212836864

; template <class P, bool ALIGN_EPI>
; __device__ __forceinline__ void gemm_phase(ldsp lds, ldsp tab, const P& S) {
;     ...
;             for (int t = 0; t < nt; t += 2) PG8_TRIP(t, PG8_MMA);
;     ...
;         if constexpr (!P::FP8) {
; #pragma unroll
;             for (int a = 0; a < 2; ++a)
; #pragma unroll
;                 for (int b = 0; b < 2; ++b)
; #pragma unroll
;                     for (int m = 0; m < 4; ++m)
; #pragma unroll
;                         for (int n = 0; n < 2; ++n) acc[a][b][m][n] = (f32x4){0.f, 0.f, 0.f, 0.f}; }
;         cur = nxt; cA = nA; cB = nB; ++ui;
.LBB0_997:
	s_ashr_i32 s15, s14, 31
	s_lshl_b64 s[16:17], s[14:15], 20
	s_add_u32 s16, s53, s16
	s_addc_u32 s17, s54, s17
	s_ashr_i32 s13, s12, 31
	s_lshl_b64 s[18:19], s[12:13], 17
	s_add_u32 s18, s55, s18
	v_mov_b32_e32 v4, 0
	s_addc_u32 s19, s56, s19
	s_mov_b32 s13, 0
	s_mov_b64 s[30:31], -1
	s_mov_b64 s[38:39], 0
	v_mov_b32_e32 v5, v4
	v_mov_b32_e32 v6, v4
	v_mov_b32_e32 v7, v4
	v_mov_b32_e32 v8, v4
	v_mov_b32_e32 v9, v4
	v_mov_b32_e32 v10, v4
	v_mov_b32_e32 v11, v4
	v_mov_b32_e32 v20, v4
	v_mov_b32_e32 v21, v4
	v_mov_b32_e32 v22, v4
	v_mov_b32_e32 v23, v4
	v_mov_b32_e32 v24, v4
	v_mov_b32_e32 v25, v4
	v_mov_b32_e32 v26, v4
	v_mov_b32_e32 v27, v4
	v_mov_b32_e32 v36, v4
	v_mov_b32_e32 v37, v4
	v_mov_b32_e32 v38, v4
	v_mov_b32_e32 v39, v4
	v_mov_b32_e32 v40, v4
	v_mov_b32_e32 v41, v4
	v_mov_b32_e32 v42, v4
	v_mov_b32_e32 v43, v4
	v_mov_b32_e32 v52, v4
	v_mov_b32_e32 v53, v4
	v_mov_b32_e32 v54, v4
	v_mov_b32_e32 v55, v4
	v_mov_b32_e32 v56, v4
	v_mov_b32_e32 v57, v4
	v_mov_b32_e32 v58, v4
	v_mov_b32_e32 v59, v4
	v_mov_b32_e32 v12, v4
	v_mov_b32_e32 v13, v4
	v_mov_b32_e32 v14, v4
	v_mov_b32_e32 v15, v4
	v_mov_b32_e32 v16, v4
	v_mov_b32_e32 v17, v4
	v_mov_b32_e32 v18, v4
	v_mov_b32_e32 v19, v4
	v_mov_b32_e32 v28, v4
	v_mov_b32_e32 v29, v4
	v_mov_b32_e32 v30, v4
	v_mov_b32_e32 v31, v4
	v_mov_b32_e32 v32, v4
	v_mov_b32_e32 v33, v4
	v_mov_b32_e32 v34, v4
	v_mov_b32_e32 v35, v4
	v_mov_b32_e32 v44, v4
	v_mov_b32_e32 v45, v4
	v_mov_b32_e32 v46, v4
	v_mov_b32_e32 v47, v4
	v_mov_b32_e32 v48, v4
	v_mov_b32_e32 v49, v4
	v_mov_b32_e32 v50, v4
	v_mov_b32_e32 v51, v4
	v_mov_b32_e32 v60, v4
	v_mov_b32_e32 v61, v4
	v_mov_b32_e32 v62, v4
	v_mov_b32_e32 v63, v4
	v_mov_b32_e32 v64, v4
	v_mov_b32_e32 v65, v4
	v_mov_b32_e32 v66, v4
	v_mov_b32_e32 v67, v4
	v_mov_b32_e32 v68, v4
	v_mov_b32_e32 v69, v4
	v_mov_b32_e32 v70, v4
	v_mov_b32_e32 v71, v4
	v_mov_b32_e32 v72, v4
	v_mov_b32_e32 v73, v4
	v_mov_b32_e32 v74, v4
	v_mov_b32_e32 v75, v4
	v_mov_b32_e32 v84, v4
	v_mov_b32_e32 v85, v4
	v_mov_b32_e32 v86, v4
	v_mov_b32_e32 v87, v4
	v_mov_b32_e32 v88, v4
	v_mov_b32_e32 v89, v4
	v_mov_b32_e32 v90, v4
	v_mov_b32_e32 v91, v4
	v_mov_b32_e32 v100, v4
	v_mov_b32_e32 v101, v4
	v_mov_b32_e32 v102, v4
	v_mov_b32_e32 v103, v4
	v_mov_b32_e32 v104, v4
	v_mov_b32_e32 v105, v4
	v_mov_b32_e32 v106, v4
	v_mov_b32_e32 v107, v4
	v_mov_b32_e32 v116, v4
	v_mov_b32_e32 v117, v4
	v_mov_b32_e32 v118, v4
	v_mov_b32_e32 v119, v4
	v_mov_b32_e32 v120, v4
	v_mov_b32_e32 v121, v4
	v_mov_b32_e32 v122, v4
	v_mov_b32_e32 v123, v4
	v_mov_b32_e32 v76, v4
	v_mov_b32_e32 v77, v4
	v_mov_b32_e32 v78, v4
	v_mov_b32_e32 v79, v4
	v_mov_b32_e32 v80, v4
	v_mov_b32_e32 v81, v4
	v_mov_b32_e32 v82, v4
	v_mov_b32_e32 v83, v4
	v_mov_b32_e32 v92, v4
	v_mov_b32_e32 v93, v4
	v_mov_b32_e32 v94, v4
	v_mov_b32_e32 v95, v4
	v_mov_b32_e32 v96, v4
	v_mov_b32_e32 v97, v4
	v_mov_b32_e32 v98, v4
	v_mov_b32_e32 v99, v4
	v_mov_b32_e32 v108, v4
	v_mov_b32_e32 v109, v4
	v_mov_b32_e32 v110, v4
	v_mov_b32_e32 v111, v4
	v_mov_b32_e32 v112, v4
	v_mov_b32_e32 v113, v4
	v_mov_b32_e32 v114, v4
	v_mov_b32_e32 v115, v4
	v_mov_b32_e32 v124, v4
	v_mov_b32_e32 v125, v4
	v_mov_b32_e32 v126, v4
	v_mov_b32_e32 v127, v4
	v_mov_b32_e32 v128, v4
	v_mov_b32_e32 v129, v4
	v_mov_b32_e32 v130, v4
	v_mov_b32_e32 v131, v4
	.p2alignl 6, 3212836864

; template <class P, bool ALIGN_EPI>
; __device__ __forceinline__ void gemm_phase(ldsp lds, ldsp tab, const P& S) {
;     ...
;             for (int t = 0; t < nt; t += 2) PG8_TRIP(t, PG8_MMA);
;     ...
;         if constexpr (!P::FP8) {
; #pragma unroll
;             for (int a = 0; a < 2; ++a)
; #pragma unroll
;                 for (int b = 0; b < 2; ++b)
; #pragma unroll
;                     for (int m = 0; m < 4; ++m)
; #pragma unroll
;                         for (int n = 0; n < 2; ++n) acc[a][b][m][n] = (f32x4){0.f, 0.f, 0.f, 0.f}; }
;         cur = nxt; cA = nA; cB = nB; ++ui;
.LBB0_1031:
	s_ashr_i32 s19, s18, 31
	s_lshl_b64 s[22:23], s[18:19], 20
	s_add_u32 s22, s49, s22
	s_addc_u32 s23, s50, s23
	v_mov_b32_e32 v127, 0
	s_andn2_b64 vcc, exec, s[14:15]
	s_cbranch_vccnz .LBB0_1041
	v_mov_b32_e32 v4, 0
	s_mov_b32 s19, 0
	s_mov_b64 s[42:43], 0x80080
	v_mov_b32_e32 v5, v4
	v_mov_b32_e32 v6, v4
	v_mov_b32_e32 v7, v4
	v_mov_b32_e32 v8, v4
	v_mov_b32_e32 v9, v4
	v_mov_b32_e32 v10, v4
	v_mov_b32_e32 v11, v4
	v_mov_b32_e32 v20, v4
	v_mov_b32_e32 v21, v4
	v_mov_b32_e32 v22, v4
	v_mov_b32_e32 v23, v4
	v_mov_b32_e32 v24, v4
	v_mov_b32_e32 v25, v4
	v_mov_b32_e32 v26, v4
	v_mov_b32_e32 v27, v4
	v_mov_b32_e32 v36, v4
	v_mov_b32_e32 v37, v4
	v_mov_b32_e32 v38, v4
	v_mov_b32_e32 v39, v4
	v_mov_b32_e32 v40, v4
	v_mov_b32_e32 v41, v4
	v_mov_b32_e32 v42, v4
	v_mov_b32_e32 v43, v4
	v_mov_b32_e32 v52, v4
	v_mov_b32_e32 v53, v4
	v_mov_b32_e32 v54, v4
	v_mov_b32_e32 v55, v4
	v_mov_b32_e32 v56, v4
	v_mov_b32_e32 v57, v4
	v_mov_b32_e32 v58, v4
	v_mov_b32_e32 v59, v4
	v_mov_b32_e32 v12, v4
	v_mov_b32_e32 v13, v4
	v_mov_b32_e32 v14, v4
	v_mov_b32_e32 v15, v4
	v_mov_b32_e32 v16, v4
	v_mov_b32_e32 v17, v4
	v_mov_b32_e32 v18, v4
	v_mov_b32_e32 v19, v4
	v_mov_b32_e32 v28, v4
	v_mov_b32_e32 v29, v4
	v_mov_b32_e32 v30, v4
	v_mov_b32_e32 v31, v4
	v_mov_b32_e32 v32, v4
	v_mov_b32_e32 v33, v4
	v_mov_b32_e32 v34, v4
	v_mov_b32_e32 v35, v4
	v_mov_b32_e32 v44, v4
	v_mov_b32_e32 v45, v4
	v_mov_b32_e32 v46, v4
	v_mov_b32_e32 v47, v4
	v_mov_b32_e32 v48, v4
	v_mov_b32_e32 v49, v4
	v_mov_b32_e32 v50, v4
	v_mov_b32_e32 v51, v4
	v_mov_b32_e32 v60, v4
	v_mov_b32_e32 v61, v4
	v_mov_b32_e32 v62, v4
	v_mov_b32_e32 v63, v4
	v_mov_b32_e32 v64, v4
	v_mov_b32_e32 v65, v4
	v_mov_b32_e32 v66, v4
	v_mov_b32_e32 v67, v4
	v_mov_b32_e32 v68, v4
	v_mov_b32_e32 v69, v4
	v_mov_b32_e32 v70, v4
	v_mov_b32_e32 v71, v4
	v_mov_b32_e32 v72, v4
	v_mov_b32_e32 v73, v4
	v_mov_b32_e32 v74, v4
	v_mov_b32_e32 v75, v4
	v_mov_b32_e32 v84, v4
	v_mov_b32_e32 v85, v4
	v_mov_b32_e32 v86, v4
	v_mov_b32_e32 v87, v4
	v_mov_b32_e32 v88, v4
	v_mov_b32_e32 v89, v4
	v_mov_b32_e32 v90, v4
	v_mov_b32_e32 v91, v4
	v_mov_b32_e32 v100, v4
	v_mov_b32_e32 v101, v4
	v_mov_b32_e32 v102, v4
	v_mov_b32_e32 v103, v4
	v_mov_b32_e32 v104, v4
	v_mov_b32_e32 v105, v4
	v_mov_b32_e32 v106, v4
	v_mov_b32_e32 v107, v4
	v_mov_b32_e32 v116, v4
	v_mov_b32_e32 v117, v4
	v_mov_b32_e32 v118, v4
	v_mov_b32_e32 v119, v4
	v_mov_b32_e32 v120, v4
	v_mov_b32_e32 v121, v4
	v_mov_b32_e32 v122, v4
	v_mov_b32_e32 v123, v4
	v_mov_b32_e32 v76, v4
	v_mov_b32_e32 v77, v4
	v_mov_b32_e32 v78, v4
	v_mov_b32_e32 v79, v4
	v_mov_b32_e32 v80, v4
	v_mov_b32_e32 v81, v4
	v_mov_b32_e32 v82, v4
	v_mov_b32_e32 v83, v4
	v_mov_b32_e32 v92, v4
	v_mov_b32_e32 v93, v4
	v_mov_b32_e32 v94, v4
	v_mov_b32_e32 v95, v4
	v_mov_b32_e32 v96, v4
	v_mov_b32_e32 v97, v4
	v_mov_b32_e32 v98, v4
	v_mov_b32_e32 v99, v4
	v_mov_b32_e32 v108, v4
	v_mov_b32_e32 v109, v4
	v_mov_b32_e32 v110, v4
	v_mov_b32_e32 v111, v4
	v_mov_b32_e32 v112, v4
	v_mov_b32_e32 v113, v4
	v_mov_b32_e32 v114, v4
	v_mov_b32_e32 v115, v4
	v_mov_b32_e32 v128, v4
	v_mov_b32_e32 v129, v4
	v_mov_b32_e32 v130, v4
	v_mov_b32_e32 v131, v4
	v_mov_b32_e32 v124, v4
	v_mov_b32_e32 v125, v4
	v_mov_b32_e32 v126, v4
	v_mov_b32_e32 v127, v4
	.p2alignl 6, 3212836864

; #define SB_DMA(t, s) do { glds(ksrc + (size_t)(t) * 64 * INP, shm + (s) * KS_SB + wid * 1024); glds(vsrc + (size_t)(t) * 64 * INP, shm + SB_VOFF + (s) * VS + wid * 1024); } while (0)
; #define SB_WAITBAR() asm volatile("s_waitcnt vmcnt(4) lgkmcnt(0)\n\ts_barrier" ::: "memory")
; __device__ __forceinline__ void sb_unit(int b, int h, int qb, const bf16_t* __restrict__ PROJ, bf16_t* OCAT, float* SSQO, ldsp shm, volatile LAS unsigned* FL) {
;     ...
;     for (int t = tmax; t >= 0; --t, ++step) {
;         SB_WAITBAR();
;         if (step > 0) { if (FL[(step - 1) % 3] == 0xFFu) break; }
;         if (tid == 0) FL[(step + 1) % 3] = 0u;
;         SB_DMA(SB_TILE(step + 3), (step + 3) & 3);
;         if (t <= tdw && !wfin) {
.LBB0_1049:
	s_and_b64 vcc, exec, s[4:5]
	s_cbranch_vccnz .LBB0_1065
	.p2alignl 6, 3212836864

; #define LAS __attribute__((address_space(3)))
; __device__ __forceinline__ float ex2(float x) { return __builtin_amdgcn_exp2f(x); }
; __device__ __forceinline__ f32x16 mfma32(bf16x8 a, bf16x8 b, f32x16 c) { return __builtin_amdgcn_mfma_f32_32x32x16_bf16(a, b, c, 0, 0, 0); }
; #define MLA_WAITBAR() do { if (wid < 4) asm volatile("s_waitcnt vmcnt(6) lgkmcnt(0)\n\ts_barrier" ::: "memory"); else asm volatile("s_waitcnt vmcnt(4) lgkmcnt(0)\n\ts_barrier" ::: "memory"); } while (0)
; #define MLA_ISSUE(s) do { const int tk_ = (s) + 3 < NT - 1 ? (s) + 3 : NT - 1, tv_ = (s) + 2 < 0 ? 0 : ((s) + 2 < NT - 1 ? (s) + 2 : NT - 1); MLA_DMAK(tk_, ((s) + 3) & 3); MLA_DMAV(tv_, ((s) + 2) & 3); } while (0)
; #define PIN(x) asm volatile("" : "+v"(x))
; __device__ __forceinline__ void mla_unit(int b, int h, int qb, const bf16_t* __restrict__ Q, const bf16_t* __restrict__ KV, const bf16_t* __restrict__ PROJ, bf16_t* OCAT, float* SSQO, ldsp shm) {
;     ...
;     MLA_WAITBAR();
;     MLA_ISSUE(0);
;     { const LAS unsigned char* kb = kp0; pA0 = f32x16{}; pA1 = f32x16{};
; #pragma unroll
;       for (int d0 = 0; d0 < 6; ++d0) { const bf16x8 k0 = *(const LAS bf16x8*)(kb + d0 * 2048), k1 = *(const LAS bf16x8*)(kb + d0 * 2048 + 512); pA0 = mfma32(k0, qr[d0], pA0); pA1 = mfma32(k1, qr[d0], pA1); }
;       mhat = rowmax(pA0, pA1);
; #pragma unroll
;       for (int r = 0; r < 16; ++r) { negm[r] = -mhat; pA0[r] = ex2(pA0[r] - mhat); pA1[r] = ex2(pA1[r] - mhat); } }
;     PIN(negm);
.LBB0_1145:
	s_mov_b64 s[10:11], 0x40000
	v_lshlrev_b32_e32 v6, 10, v184
	v_lshlrev_b32_e32 v7, 4, v183
	v_lshl_add_u64 v[4:5], v[4:5], 0, s[10:11]
	s_add_i32 m0, s26, 0x10000
	v_add3_u32 v188, 0, v6, v7
	global_load_lds_dwordx4 v[4:5], off
	ds_read_b128 v[4:7], v188
	ds_read_b128 v[10:13], v188 offset:512
	s_waitcnt vmcnt(0) lgkmcnt(0)
	v_mfma_f32_32x32x16_bf16 v[20:35], v[4:7], v[136:139], 0
	v_lshlrev_b32_e32 v9, 8, v184
	s_and_b32 s8, s2, 0x3fffffc0
	s_lshl_b32 s8, s8, 2
	s_add_i32 s51, s8, 0
	s_mov_b32 s8, s9
	s_mov_b32 s10, s9
	s_mov_b32 s11, s9
	v_mfma_f32_32x32x16_bf16 v[52:67], v[10:13], v[136:139], 0
	ds_read_b128 v[4:7], v188 offset:2048
	ds_read_b128 v[10:13], v188 offset:2560
	s_mov_b32 s12, s9
	s_mov_b32 s13, s9
	s_mov_b32 s14, s9
	s_mov_b32 s15, s9
	s_mov_b32 s16, s9
	s_mov_b32 s17, s9
	s_waitcnt lgkmcnt(1)
	v_mfma_f32_32x32x16_bf16 v[20:35], v[4:7], v[132:135], v[20:35]
	s_mov_b32 s18, s9
	s_mov_b32 s19, s9
	s_mov_b32 s20, s9
	s_mov_b32 s21, s9
	s_mov_b32 s22, s9
	s_mov_b32 s23, s9
	s_lshl_b32 s3, s3, 2
	s_waitcnt lgkmcnt(0)
	v_mfma_f32_32x32x16_bf16 v[52:67], v[10:13], v[132:135], v[52:67]
	ds_read_b128 v[4:7], v188 offset:4096
	ds_read_b128 v[10:13], v188 offset:4608
	s_ashr_i32 s2, s2, 7
	s_add_i32 s51, s51, 0x14000
	s_add_i32 s52, s2, s3
	s_mov_b32 s27, 2
	s_add_i32 s52, s52, 1
	s_or_b32 s2, s3, 3
	s_waitcnt lgkmcnt(1)
	v_mfma_f32_32x32x16_bf16 v[20:35], v[4:7], v[128:131], v[20:35]
	ds_read_b128 v[4:7], v188 offset:6144
	ds_read_b128 v[36:39], v188 offset:10752
	v_cmp_gt_u32_e64 s[36:37], 32, v182
	v_lshl_add_u32 v185, v183, 2, s51
	v_mov_b32_e32 v189, 0
	s_waitcnt lgkmcnt(2)
	v_mfma_f32_32x32x16_bf16 v[52:67], v[10:13], v[128:131], v[52:67]
	ds_read_b128 v[10:13], v188 offset:6656
	s_waitcnt lgkmcnt(2)
	v_mfma_f32_32x32x16_bf16 v[20:35], v[4:7], v[124:127], v[20:35]
	v_lshlrev_b32_e32 v4, 1, v1
	v_and_b32_e32 v4, 32, v4
	v_add3_u32 v8, 0, v4, v8
	v_lshlrev_b32_e32 v4, 4, v1
	v_and_b32_e32 v14, 0xc0, v4
	ds_read_b128 v[4:7], v188 offset:8192
	v_add3_u32 v186, v8, v9, v14
	s_waitcnt lgkmcnt(1)
	v_mfma_f32_32x32x16_bf16 v[52:67], v[10:13], v[124:127], v[52:67]
	ds_read_b128 v[8:11], v188 offset:8704
	s_waitcnt lgkmcnt(1)
	v_mfma_f32_32x32x16_bf16 v[20:35], v[4:7], v[120:123], v[20:35]
	ds_read_b128 v[4:7], v188 offset:10240
	s_waitcnt lgkmcnt(1)
	v_mfma_f32_32x32x16_bf16 v[52:67], v[8:11], v[120:123], v[52:67]
	s_waitcnt lgkmcnt(0)
	v_mfma_f32_32x32x16_bf16 v[20:35], v[4:7], v[116:119], v[20:35]
	v_mov_b64_e32 v[4:5], s[8:9]
	v_mov_b64_e32 v[18:19], s[22:23]
	v_mov_b64_e32 v[6:7], s[10:11]
	v_mov_b64_e32 v[8:9], s[12:13]
	v_mov_b64_e32 v[10:11], s[14:15]
	v_mov_b64_e32 v[12:13], s[16:17]
	v_mov_b64_e32 v[14:15], s[18:19]
	v_mfma_f32_32x32x16_bf16 v[52:67], v[36:39], v[116:119], v[52:67]
	s_nop 3
	v_max_f32_e32 v40, v21, v21
	v_max_f32_e32 v41, v20, v20
	v_max_f32_e32 v40, v41, v40
	v_mov_b64_e32 v[16:17], s[20:21]
	s_mov_b32 s14, 0x8000
	s_nop 2
	v_max3_f32 v36, v22, v23, v53
	v_max3_f32 v37, v40, v52, v54
	v_max3_f32 v37, v37, v55, v24
	v_max3_f32 v36, v36, v26, v27
	v_max3_f32 v37, v37, v25, v56
	v_max3_f32 v36, v36, v58, v59
	v_max3_f32 v37, v37, v57, v28
	v_max3_f32 v36, v36, v30, v31
	v_max3_f32 v37, v37, v29, v60
	v_max3_f32 v36, v36, v62, v63
	v_max3_f32 v37, v37, v61, v32
	v_max3_f32 v36, v36, v34, v35
	v_max3_f32 v37, v37, v33, v64
	v_max3_f32 v36, v36, v66, v67
	v_max3_f32 v36, v37, v65, v36
	v_mov_b32_e32 v37, v36
	s_nop 1
	v_permlane32_swap_b32_e32 v36, v37
	v_max_f32_e32 v37, v37, v37
	v_max_f32_e32 v36, v36, v36
	v_max_f32_e32 v187, v36, v37
	v_sub_f32_e32 v20, v20, v187
	v_exp_f32_e32 v68, v20
	v_sub_f32_e32 v20, v21, v187
	v_exp_f32_e32 v69, v20
	v_sub_f32_e32 v20, v22, v187
	v_exp_f32_e32 v70, v20
	v_sub_f32_e32 v20, v23, v187
	v_exp_f32_e32 v71, v20
	v_sub_f32_e32 v20, v24, v187
	v_exp_f32_e32 v72, v20
	v_sub_f32_e32 v20, v25, v187
	v_exp_f32_e32 v73, v20
	v_sub_f32_e32 v20, v26, v187
	v_exp_f32_e32 v74, v20
	v_sub_f32_e32 v20, v27, v187
	v_exp_f32_e32 v75, v20
	v_sub_f32_e32 v20, v28, v187
	v_exp_f32_e32 v76, v20
	v_sub_f32_e32 v20, v29, v187
	v_exp_f32_e32 v77, v20
	v_sub_f32_e32 v20, v30, v187
	v_exp_f32_e32 v78, v20
	v_sub_f32_e32 v20, v31, v187
	v_exp_f32_e32 v79, v20
	v_sub_f32_e32 v20, v32, v187
	v_exp_f32_e32 v80, v20
	v_sub_f32_e32 v20, v33, v187
	v_exp_f32_e32 v81, v20
	v_sub_f32_e32 v20, v34, v187
	v_sub_f32_e32 v52, v52, v187
	v_sub_f32_e32 v53, v53, v187
	v_sub_f32_e32 v54, v54, v187
	v_sub_f32_e32 v55, v55, v187
	v_sub_f32_e32 v56, v56, v187
	v_sub_f32_e32 v57, v57, v187
	v_sub_f32_e32 v58, v58, v187
	v_sub_f32_e32 v59, v59, v187
	v_sub_f32_e32 v60, v60, v187
	v_sub_f32_e32 v61, v61, v187
	v_sub_f32_e32 v62, v62, v187
	v_sub_f32_e32 v63, v63, v187
	v_sub_f32_e32 v64, v64, v187
	v_sub_f32_e32 v65, v65, v187
	v_sub_f32_e32 v66, v66, v187
	v_sub_f32_e32 v67, v67, v187
	v_exp_f32_e32 v82, v20
	v_sub_f32_e32 v20, v35, v187
	v_exp_f32_e32 v52, v52
	v_exp_f32_e32 v53, v53
	v_exp_f32_e32 v54, v54
	v_exp_f32_e32 v55, v55
	v_exp_f32_e32 v56, v56
	v_exp_f32_e32 v57, v57
	v_exp_f32_e32 v58, v58
	v_exp_f32_e32 v59, v59
	v_exp_f32_e32 v83, v20
	v_xor_b32_e32 v36, 0x80000000, v187
	v_mov_b64_e32 v[34:35], v[18:19]
	v_mov_b32_e32 v37, v36
	v_mov_b32_e32 v38, v36
	v_mov_b32_e32 v39, v36
	v_mov_b32_e32 v40, v36
	v_mov_b32_e32 v41, v36
	v_mov_b32_e32 v42, v36
	v_mov_b32_e32 v43, v36
	v_mov_b32_e32 v44, v36
	v_mov_b32_e32 v45, v36
	v_mov_b32_e32 v46, v36
	v_mov_b32_e32 v47, v36
	v_mov_b32_e32 v48, v36
	v_mov_b32_e32 v49, v36
	v_mov_b32_e32 v50, v36
	v_mov_b32_e32 v51, v36
	v_mov_b64_e32 v[32:33], v[16:17]
	v_mov_b64_e32 v[30:31], v[14:15]
	v_mov_b64_e32 v[28:29], v[12:13]
	v_mov_b64_e32 v[26:27], v[10:11]
	v_mov_b64_e32 v[24:25], v[8:9]
	v_mov_b64_e32 v[22:23], v[6:7]
	v_mov_b64_e32 v[20:21], v[4:5]
	s_add_i32 s12, s27, -1
	s_and_b32 s12, s12, 3
	s_mulk_i32 s12, 0x3000
	v_add_u32_e32 v156, s12, v188
	s_and_b32 s12, s14, 0x6000
	v_add_u32_e32 v157, s12, v186
	ds_read_b128 v[202:205], v156
	ds_read_b128 v[190:193], v156 offset:512
	ds_read_b128 v[194:197], v156 offset:2048
	ds_read_b128 v[198:201], v156 offset:2560
	.p2alignl 6, 3212836864

; template <class P, bool ALIGN_EPI>
; __device__ __forceinline__ void gemm_phase(ldsp lds, ldsp tab, const P& S) {
;     ...
;             for (int t = 2; t < nt; t += 2) PG8_TRIP(t, PG8_MMA);
;         } else {
;             for (int t = 0; t < nt; t += 2) PG8_TRIP(t, PG8_MMA);
.LBB0_1275:
	s_add_i32 s3, s3, 2
	s_add_u32 s42, s42, 0x100
	s_addc_u32 s43, s43, 0
	s_cmp_gt_u32 s3, 13
	s_cbranch_scc1 .LBB0_1278
	.p2alignl 6, 3212836864

; template <class P, bool ALIGN_EPI>
; __device__ __forceinline__ void gemm_phase(ldsp lds, ldsp tab, const P& S) {
;     ...
;         if constexpr (P::FP8) {
;             PG8_TRIP(0, PG8_MMAZ);
.LBB0_1606:
	s_add_i32 s26, 0, 0x10000
	s_add_i32 s28, 0, 0x14000
	v_add_u32_e32 v167, s26, v187
	v_add_u32_e32 v173, s28, v187
	ds_read_b128 v[4:7], v167
	s_waitcnt vmcnt(0)
	ds_read_b128 v[8:11], v167 offset:1024
	ds_read_b128 v[12:15], v167 offset:2048
	ds_read_b128 v[16:19], v167 offset:3072
	s_waitcnt vmcnt(0)
	ds_read_b128 v[20:23], v173
	ds_read_b128 v[24:27], v173 offset:1024
	ds_read_b128 v[28:31], v173 offset:2048
	ds_read_b128 v[32:35], v173 offset:3072
	v_mov_b32_e32 v171, v3
	v_mov_b32_e32 v169, v3
	s_add_i32 s3, s67, 0xc000
	s_mov_b32 m0, s3
	s_add_i32 s13, s67, 0xe000
	ds_read_b128 v[36:39], v175
	ds_read_b128 v[40:43], v175 offset:1024
	ds_read_b128 v[44:47], v175 offset:2048
	ds_read_b128 v[48:51], v175 offset:3072
	ds_read_b128 v[52:55], v175 offset:4096
	ds_read_b128 v[56:59], v175 offset:5120
	ds_read_b128 v[60:63], v175 offset:6144
	ds_read_b128 v[64:67], v175 offset:7168
	global_load_lds_dwordx4 v170, s[18:19]
	s_mov_b32 m0, s13
	s_nop 0
	global_load_lds_dwordx4 v168, s[18:19]
	s_waitcnt vmcnt(8)
	s_waitcnt lgkmcnt(0)
	s_barrier
	s_setprio 1
	s_waitcnt lgkmcnt(0)
	v_mfma_scale_f32_16x16x128_f8f6f4 v[156:159], v[4:11], v[36:43], 0, v243, v243 op_sel_hi:[0,0,0]
	v_mfma_scale_f32_16x16x128_f8f6f4 v[160:163], v[12:19], v[36:43], 0, v243, v243 op_sel_hi:[0,0,0]
	v_mfma_scale_f32_16x16x128_f8f6f4 v[140:143], v[4:11], v[44:51], 0, v243, v243 op_sel_hi:[0,0,0]
	v_mfma_scale_f32_16x16x128_f8f6f4 v[144:147], v[12:19], v[44:51], 0, v243, v243 op_sel_hi:[0,0,0]
	v_mfma_scale_f32_16x16x128_f8f6f4 v[124:127], v[4:11], v[52:59], 0, v243, v243 op_sel_hi:[0,0,0]
	v_mfma_scale_f32_16x16x128_f8f6f4 v[128:131], v[12:19], v[52:59], 0, v243, v243 op_sel_hi:[0,0,0]
	v_mfma_scale_f32_16x16x128_f8f6f4 v[108:111], v[4:11], v[60:67], 0, v243, v243 op_sel_hi:[0,0,0]
	v_mfma_scale_f32_16x16x128_f8f6f4 v[112:115], v[12:19], v[60:67], 0, v243, v243 op_sel_hi:[0,0,0]
	s_setprio 0
	s_setprio 1
	v_mfma_scale_f32_16x16x128_f8f6f4 v[148:151], v[20:27], v[36:43], 0, v243, v243 op_sel_hi:[0,0,0]
	v_mfma_scale_f32_16x16x128_f8f6f4 v[152:155], v[28:35], v[36:43], 0, v243, v243 op_sel_hi:[0,0,0]
	v_mfma_scale_f32_16x16x128_f8f6f4 v[132:135], v[20:27], v[44:51], 0, v243, v243 op_sel_hi:[0,0,0]
	v_mfma_scale_f32_16x16x128_f8f6f4 v[136:139], v[28:35], v[44:51], 0, v243, v243 op_sel_hi:[0,0,0]
	v_mfma_scale_f32_16x16x128_f8f6f4 v[116:119], v[20:27], v[52:59], 0, v243, v243 op_sel_hi:[0,0,0]
	v_mfma_scale_f32_16x16x128_f8f6f4 v[120:123], v[28:35], v[52:59], 0, v243, v243 op_sel_hi:[0,0,0]
	v_mfma_scale_f32_16x16x128_f8f6f4 v[100:103], v[20:27], v[60:67], 0, v243, v243 op_sel_hi:[0,0,0]
	v_mfma_scale_f32_16x16x128_f8f6f4 v[104:107], v[28:35], v[60:67], 0, v243, v243 op_sel_hi:[0,0,0]
	s_setprio 0
	s_barrier
	v_lshl_add_u64 v[176:177], s[48:49], 0, v[2:3]
	s_mov_b64 s[34:35], 0x100
	s_add_i32 s26, s26, s66
	v_mov_b32_e32 v165, v3
	v_lshl_add_u64 v[36:37], v[176:177], 0, s[34:35]
	s_mov_b32 m0, s26
	v_lshl_add_u64 v[178:179], s[48:49], 0, v[164:165]
	s_add_i32 s27, s26, 0x2000
	ds_read_b128 v[48:51], v175 offset:16384
	ds_read_b128 v[52:55], v175 offset:17408
	ds_read_b128 v[194:197], v175 offset:18432
	ds_read_b128 v[198:201], v175 offset:19456
	ds_read_b128 v[202:205], v175 offset:20480
	ds_read_b128 v[206:209], v175 offset:21504
	ds_read_b128 v[216:219], v175 offset:22528
	ds_read_b128 v[220:223], v175 offset:23552
	global_load_lds_dwordx4 v[36:37], off
	v_lshl_add_u64 v[36:37], v[178:179], 0, s[34:35]
	s_add_u32 s34, s48, 0x20100
	s_mov_b32 m0, s27
	s_addc_u32 s35, s49, 0
	s_add_i32 s28, s28, s66
	global_load_lds_dwordx4 v[36:37], off
	s_mov_b32 m0, s28
	s_add_i32 s33, s28, 0x2000
	global_load_lds_dwordx4 v2, s[34:35]
	s_mov_b32 m0, s33
	s_nop 0
	global_load_lds_dwordx4 v164, s[34:35]
	s_mov_b32 m0, s67
	s_nop 0
	global_load_lds_dwordx4 v174, s[22:23]
	s_mov_b32 m0, s68
	s_nop 0
	global_load_lds_dwordx4 v172, s[22:23]
	s_waitcnt vmcnt(8)
	s_waitcnt lgkmcnt(0)
	s_barrier
	s_setprio 1
	s_waitcnt lgkmcnt(0)
	v_mfma_scale_f32_16x16x128_f8f6f4 v[92:95], v[4:11], v[48:55], 0, v243, v243 op_sel_hi:[0,0,0]
	v_mfma_scale_f32_16x16x128_f8f6f4 v[96:99], v[12:19], v[48:55], 0, v243, v243 op_sel_hi:[0,0,0]
	v_mfma_scale_f32_16x16x128_f8f6f4 v[76:79], v[4:11], v[194:201], 0, v243, v243 op_sel_hi:[0,0,0]
	v_mfma_scale_f32_16x16x128_f8f6f4 v[80:83], v[12:19], v[194:201], 0, v243, v243 op_sel_hi:[0,0,0]
	v_mfma_scale_f32_16x16x128_f8f6f4 v[60:63], v[4:11], v[202:209], 0, v243, v243 op_sel_hi:[0,0,0]
	v_mfma_scale_f32_16x16x128_f8f6f4 v[64:67], v[12:19], v[202:209], 0, v243, v243 op_sel_hi:[0,0,0]
	v_mfma_scale_f32_16x16x128_f8f6f4 v[40:43], v[4:11], v[216:223], 0, v243, v243 op_sel_hi:[0,0,0]
	v_mfma_scale_f32_16x16x128_f8f6f4 v[44:47], v[12:19], v[216:223], 0, v243, v243 op_sel_hi:[0,0,0]
	s_setprio 0
	s_setprio 1
	v_mfma_scale_f32_16x16x128_f8f6f4 v[84:87], v[20:27], v[48:55], 0, v243, v243 op_sel_hi:[0,0,0]
	v_mfma_scale_f32_16x16x128_f8f6f4 v[88:91], v[28:35], v[48:55], 0, v243, v243 op_sel_hi:[0,0,0]
	v_mfma_scale_f32_16x16x128_f8f6f4 v[68:71], v[20:27], v[194:201], 0, v243, v243 op_sel_hi:[0,0,0]
	v_mfma_scale_f32_16x16x128_f8f6f4 v[72:75], v[28:35], v[194:201], 0, v243, v243 op_sel_hi:[0,0,0]
	v_mfma_scale_f32_16x16x128_f8f6f4 v[52:55], v[20:27], v[202:209], 0, v243, v243 op_sel_hi:[0,0,0]
	v_mfma_scale_f32_16x16x128_f8f6f4 v[56:59], v[28:35], v[202:209], 0, v243, v243 op_sel_hi:[0,0,0]
	v_mfma_scale_f32_16x16x128_f8f6f4 v[36:39], v[20:27], v[216:223], 0, v243, v243 op_sel_hi:[0,0,0]
	v_mfma_scale_f32_16x16x128_f8f6f4 v[48:51], v[28:35], v[216:223], 0, v243, v243 op_sel_hi:[0,0,0]
	s_setprio 0
	s_barrier
; template <class P, bool ALIGN_EPI>
; __device__ __forceinline__ void gemm_phase(ldsp lds, ldsp tab, const P& S) {
;     ...
;             PG8_TRIP(0, PG8_MMAZ);
;             for (int t = 2; t < nt; t += 2) PG8_TRIP(t, PG8_MMA);
	s_add_i32 s34, 0, 0x18000
	s_add_i32 s41, 0, 0x1c000
	v_add_u32_e32 v193, s34, v187
	v_add_u32_e32 v194, s41, v187
	ds_read_b128 v[28:31], v193
	ds_read_b128 v[32:35], v193 offset:1024
	ds_read_b128 v[20:23], v193 offset:2048
	ds_read_b128 v[24:27], v193 offset:3072
	ds_read_b128 v[12:15], v194
	ds_read_b128 v[16:19], v194 offset:1024
	ds_read_b128 v[4:7], v194 offset:2048
	ds_read_b128 v[8:11], v194 offset:3072
	s_mov_b32 m0, s69
	ds_read_b128 v[196:199], v175 offset:32768
	ds_read_b128 v[200:203], v175 offset:33792
	ds_read_b128 v[204:207], v175 offset:34816
	ds_read_b128 v[208:211], v175 offset:35840
	ds_read_b128 v[216:219], v175 offset:36864
	ds_read_b128 v[220:223], v175 offset:37888
	ds_read_b128 v[224:227], v175 offset:38912
	ds_read_b128 v[228:231], v175 offset:39936
	global_load_lds_dwordx4 v170, s[22:23]
	s_mov_b32 m0, s70
	s_nop 0
	global_load_lds_dwordx4 v168, s[22:23]
	s_waitcnt vmcnt(8)
	s_waitcnt lgkmcnt(0)
	s_barrier
	s_setprio 1
	s_waitcnt lgkmcnt(0)
	v_mfma_scale_f32_16x16x128_f8f6f4 v[156:159], v[28:35], v[196:203], v[156:159], v243, v243 op_sel_hi:[0,0,0]
	v_mfma_scale_f32_16x16x128_f8f6f4 v[160:163], v[20:27], v[196:203], v[160:163], v243, v243 op_sel_hi:[0,0,0]
	v_mfma_scale_f32_16x16x128_f8f6f4 v[140:143], v[28:35], v[204:211], v[140:143], v243, v243 op_sel_hi:[0,0,0]
	v_mfma_scale_f32_16x16x128_f8f6f4 v[144:147], v[20:27], v[204:211], v[144:147], v243, v243 op_sel_hi:[0,0,0]
	v_mfma_scale_f32_16x16x128_f8f6f4 v[124:127], v[28:35], v[216:223], v[124:127], v243, v243 op_sel_hi:[0,0,0]
	v_mfma_scale_f32_16x16x128_f8f6f4 v[128:131], v[20:27], v[216:223], v[128:131], v243, v243 op_sel_hi:[0,0,0]
	v_mfma_scale_f32_16x16x128_f8f6f4 v[108:111], v[28:35], v[224:231], v[108:111], v243, v243 op_sel_hi:[0,0,0]
	v_mfma_scale_f32_16x16x128_f8f6f4 v[112:115], v[20:27], v[224:231], v[112:115], v243, v243 op_sel_hi:[0,0,0]
	s_setprio 0
	s_setprio 1
	v_mfma_scale_f32_16x16x128_f8f6f4 v[148:151], v[12:19], v[196:203], v[148:151], v243, v243 op_sel_hi:[0,0,0]
	v_mfma_scale_f32_16x16x128_f8f6f4 v[152:155], v[4:11], v[196:203], v[152:155], v243, v243 op_sel_hi:[0,0,0]
	v_mfma_scale_f32_16x16x128_f8f6f4 v[132:135], v[12:19], v[204:211], v[132:135], v243, v243 op_sel_hi:[0,0,0]
	v_mfma_scale_f32_16x16x128_f8f6f4 v[136:139], v[4:11], v[204:211], v[136:139], v243, v243 op_sel_hi:[0,0,0]
	v_mfma_scale_f32_16x16x128_f8f6f4 v[116:119], v[12:19], v[216:223], v[116:119], v243, v243 op_sel_hi:[0,0,0]
	v_mfma_scale_f32_16x16x128_f8f6f4 v[120:123], v[4:11], v[216:223], v[120:123], v243, v243 op_sel_hi:[0,0,0]
	v_mfma_scale_f32_16x16x128_f8f6f4 v[100:103], v[12:19], v[224:231], v[100:103], v243, v243 op_sel_hi:[0,0,0]
	v_mfma_scale_f32_16x16x128_f8f6f4 v[104:107], v[4:11], v[224:231], v[104:107], v243, v243 op_sel_hi:[0,0,0]
	s_setprio 0
	s_barrier
	s_mov_b64 s[46:47], 0x180
	s_add_i32 s34, s34, s66
	v_lshl_add_u64 v[176:177], v[176:177], 0, s[46:47]
	s_mov_b32 m0, s34
	s_add_i32 s35, s34, 0x2000
	ds_read_b128 v[196:199], v175 offset:49152
	ds_read_b128 v[200:203], v175 offset:50176
	ds_read_b128 v[204:207], v175 offset:51200
	ds_read_b128 v[208:211], v175 offset:52224
	ds_read_b128 v[216:219], v175 offset:53248
	ds_read_b128 v[220:223], v175 offset:54272
	ds_read_b128 v[224:227], v175 offset:55296
	ds_read_b128 v[228:231], v175 offset:56320
	global_load_lds_dwordx4 v[176:177], off
	v_lshl_add_u64 v[176:177], v[178:179], 0, s[46:47]
	s_add_u32 s46, s48, 0x20180
	s_mov_b32 m0, s35
	s_addc_u32 s47, s49, 0
	s_add_i32 s41, s41, s66
	global_load_lds_dwordx4 v[176:177], off
	s_mov_b32 m0, s41
	s_add_i32 s43, s41, 0x2000
	global_load_lds_dwordx4 v2, s[46:47]
	s_mov_b32 m0, s43
	s_nop 0
	global_load_lds_dwordx4 v164, s[46:47]
	s_mov_b32 m0, s72
	s_nop 0
	global_load_lds_dwordx4 v174, s[30:31]
	s_mov_b32 m0, s73
	s_nop 0
	global_load_lds_dwordx4 v172, s[30:31]
	s_waitcnt vmcnt(8)
	s_waitcnt lgkmcnt(0)
	s_barrier
	s_setprio 1
	s_waitcnt lgkmcnt(0)
	v_mfma_scale_f32_16x16x128_f8f6f4 v[92:95], v[28:35], v[196:203], v[92:95], v243, v243 op_sel_hi:[0,0,0]
	v_mfma_scale_f32_16x16x128_f8f6f4 v[96:99], v[20:27], v[196:203], v[96:99], v243, v243 op_sel_hi:[0,0,0]
	v_mfma_scale_f32_16x16x128_f8f6f4 v[76:79], v[28:35], v[204:211], v[76:79], v243, v243 op_sel_hi:[0,0,0]
	v_mfma_scale_f32_16x16x128_f8f6f4 v[80:83], v[20:27], v[204:211], v[80:83], v243, v243 op_sel_hi:[0,0,0]
	v_mfma_scale_f32_16x16x128_f8f6f4 v[60:63], v[28:35], v[216:223], v[60:63], v243, v243 op_sel_hi:[0,0,0]
	v_mfma_scale_f32_16x16x128_f8f6f4 v[64:67], v[20:27], v[216:223], v[64:67], v243, v243 op_sel_hi:[0,0,0]
	v_mfma_scale_f32_16x16x128_f8f6f4 v[40:43], v[28:35], v[224:231], v[40:43], v243, v243 op_sel_hi:[0,0,0]
	v_mfma_scale_f32_16x16x128_f8f6f4 v[44:47], v[20:27], v[224:231], v[44:47], v243, v243 op_sel_hi:[0,0,0]
	s_setprio 0
	s_setprio 1
	v_mfma_scale_f32_16x16x128_f8f6f4 v[84:87], v[12:19], v[196:203], v[84:87], v243, v243 op_sel_hi:[0,0,0]
	v_mfma_scale_f32_16x16x128_f8f6f4 v[88:91], v[4:11], v[196:203], v[88:91], v243, v243 op_sel_hi:[0,0,0]
	v_mfma_scale_f32_16x16x128_f8f6f4 v[68:71], v[12:19], v[204:211], v[68:71], v243, v243 op_sel_hi:[0,0,0]
	v_mfma_scale_f32_16x16x128_f8f6f4 v[72:75], v[4:11], v[204:211], v[72:75], v243, v243 op_sel_hi:[0,0,0]
	v_mfma_scale_f32_16x16x128_f8f6f4 v[52:55], v[12:19], v[216:223], v[52:55], v243, v243 op_sel_hi:[0,0,0]
	v_mfma_scale_f32_16x16x128_f8f6f4 v[56:59], v[4:11], v[216:223], v[56:59], v243, v243 op_sel_hi:[0,0,0]
	v_mfma_scale_f32_16x16x128_f8f6f4 v[36:39], v[12:19], v[224:231], v[36:39], v243, v243 op_sel_hi:[0,0,0]
	v_mfma_scale_f32_16x16x128_f8f6f4 v[48:51], v[4:11], v[224:231], v[48:51], v243, v243 op_sel_hi:[0,0,0]
	s_setprio 0
	s_barrier
	s_mov_b32 s45, 0
	s_mov_b64 s[50:51], 0x200
	s_mov_b64 s[52:53], s[30:31]
	.p2alignl 6, 3212836864

; template <class P, bool ALIGN_EPI>
; __device__ __forceinline__ void gemm_phase(ldsp lds, ldsp tab, const P& S) {
;     ...
;             PG8_TRIP(0, PG8_MMAZ);
.LBB0_1717:
	s_add_i32 s26, 0, 0x10000
	s_add_i32 s28, 0, 0x14000
	v_add_u32_e32 v173, s26, v185
	v_add_u32_e32 v187, s28, v185
	ds_read_b128 v[4:7], v173
	ds_read_b128 v[8:11], v173 offset:1024
	ds_read_b128 v[12:15], v173 offset:2048
	ds_read_b128 v[16:19], v173 offset:3072
	ds_read_b128 v[20:23], v187
	ds_read_b128 v[24:27], v187 offset:1024
	ds_read_b128 v[28:31], v187 offset:2048
	ds_read_b128 v[32:35], v187 offset:3072
	s_add_u32 s20, s16, 0x70080
	s_addc_u32 s21, s17, 0
	s_add_i32 s3, s44, 0xc000
	s_mov_b32 m0, s3
	s_add_i32 s19, s44, 0xe000
	ds_read_b128 v[36:39], v186
	ds_read_b128 v[40:43], v186 offset:1024
	ds_read_b128 v[44:47], v186 offset:2048
	ds_read_b128 v[48:51], v186 offset:3072
	ds_read_b128 v[52:55], v186 offset:4096
	ds_read_b128 v[56:59], v186 offset:5120
	ds_read_b128 v[60:63], v186 offset:6144
	ds_read_b128 v[64:67], v186 offset:7168
	global_load_lds_dwordx4 v2, s[20:21]
	s_mov_b32 m0, s19
	v_mov_b32_e32 v167, v3
	global_load_lds_dwordx4 v166, s[20:21]
	s_waitcnt vmcnt(8)
	s_waitcnt lgkmcnt(0)
	s_barrier
	s_setprio 1
	s_waitcnt lgkmcnt(0)
	v_mfma_scale_f32_16x16x128_f8f6f4 v[148:151], v[4:11], v[36:43], 0, v243, v243 op_sel_hi:[0,0,0]
	v_mfma_scale_f32_16x16x128_f8f6f4 v[152:155], v[12:19], v[36:43], 0, v243, v243 op_sel_hi:[0,0,0]
	v_mfma_scale_f32_16x16x128_f8f6f4 v[136:139], v[4:11], v[44:51], 0, v243, v243 op_sel_hi:[0,0,0]
	v_mfma_scale_f32_16x16x128_f8f6f4 v[132:135], v[12:19], v[44:51], 0, v243, v243 op_sel_hi:[0,0,0]
	v_mfma_scale_f32_16x16x128_f8f6f4 v[120:123], v[4:11], v[52:59], 0, v243, v243 op_sel_hi:[0,0,0]
	v_mfma_scale_f32_16x16x128_f8f6f4 v[116:119], v[12:19], v[52:59], 0, v243, v243 op_sel_hi:[0,0,0]
	v_mfma_scale_f32_16x16x128_f8f6f4 v[92:95], v[4:11], v[60:67], 0, v243, v243 op_sel_hi:[0,0,0]
	v_mfma_scale_f32_16x16x128_f8f6f4 v[84:87], v[12:19], v[60:67], 0, v243, v243 op_sel_hi:[0,0,0]
	s_setprio 0
	s_setprio 1
	v_mfma_scale_f32_16x16x128_f8f6f4 v[156:159], v[20:27], v[36:43], 0, v243, v243 op_sel_hi:[0,0,0]
	v_mfma_scale_f32_16x16x128_f8f6f4 v[160:163], v[28:35], v[36:43], 0, v243, v243 op_sel_hi:[0,0,0]
	v_mfma_scale_f32_16x16x128_f8f6f4 v[144:147], v[20:27], v[44:51], 0, v243, v243 op_sel_hi:[0,0,0]
	v_mfma_scale_f32_16x16x128_f8f6f4 v[140:143], v[28:35], v[44:51], 0, v243, v243 op_sel_hi:[0,0,0]
	v_mfma_scale_f32_16x16x128_f8f6f4 v[128:131], v[20:27], v[52:59], 0, v243, v243 op_sel_hi:[0,0,0]
	v_mfma_scale_f32_16x16x128_f8f6f4 v[124:127], v[28:35], v[52:59], 0, v243, v243 op_sel_hi:[0,0,0]
	v_mfma_scale_f32_16x16x128_f8f6f4 v[96:99], v[20:27], v[60:67], 0, v243, v243 op_sel_hi:[0,0,0]
	v_mfma_scale_f32_16x16x128_f8f6f4 v[88:91], v[28:35], v[60:67], 0, v243, v243 op_sel_hi:[0,0,0]
	s_setprio 0
	s_barrier
	v_mov_b32_e32 v165, v3
	v_lshl_add_u64 v[176:177], v[170:171], 0, v[164:165]
	s_mov_b64 s[22:23], 0x100
	s_add_i32 s26, s26, s43
	v_mov_b32_e32 v169, v3
	v_lshl_add_u64 v[44:45], v[176:177], 0, s[22:23]
	s_mov_b32 m0, s26
	v_lshl_add_u64 v[178:179], v[170:171], 0, v[168:169]
	s_add_i32 s27, s26, 0x2000
	ds_read_b128 v[36:39], v186 offset:16384
	ds_read_b128 v[40:43], v186 offset:17408
	ds_read_b128 v[52:55], v186 offset:18432
	ds_read_b128 v[56:59], v186 offset:19456
	ds_read_b128 v[188:191], v186 offset:20480
	ds_read_b128 v[192:195], v186 offset:21504
	ds_read_b128 v[196:199], v186 offset:22528
	ds_read_b128 v[200:203], v186 offset:23552
	global_load_lds_dwordx4 v[44:45], off
	v_lshl_add_u64 v[44:45], v[178:179], 0, s[22:23]
	s_mov_b32 m0, s27
	s_mov_b64 s[20:21], 0x70100
	global_load_lds_dwordx4 v[44:45], off
	v_lshl_add_u64 v[44:45], v[170:171], 0, s[20:21]
	s_add_i32 s28, s28, s43
	v_readfirstlane_b32 s20, v44
	v_readfirstlane_b32 s21, v45
	s_mov_b32 m0, s28
	s_add_i32 s33, s28, 0x2000
	v_lshl_add_u64 v[180:181], s[16:17], 0, v[2:3]
	v_lshl_add_u64 v[44:45], v[180:181], 0, s[22:23]
	v_lshl_add_u64 v[182:183], s[16:17], 0, v[166:167]
	global_load_lds_dwordx4 v164, s[20:21]
	s_mov_b32 m0, s33
	s_nop 0
	global_load_lds_dwordx4 v168, s[20:21]
	s_mov_b32 m0, s44
	s_nop 0
	global_load_lds_dwordx4 v[44:45], off
	v_lshl_add_u64 v[44:45], v[182:183], 0, s[22:23]
	s_mov_b32 m0, s45
	s_nop 0
	global_load_lds_dwordx4 v[44:45], off
	s_waitcnt vmcnt(8)
	s_waitcnt lgkmcnt(0)
	s_barrier
	s_setprio 1
	s_waitcnt lgkmcnt(0)
	v_mfma_scale_f32_16x16x128_f8f6f4 v[104:107], v[4:11], v[36:43], 0, v243, v243 op_sel_hi:[0,0,0]
	v_mfma_scale_f32_16x16x128_f8f6f4 v[100:103], v[12:19], v[36:43], 0, v243, v243 op_sel_hi:[0,0,0]
	v_mfma_scale_f32_16x16x128_f8f6f4 v[76:79], v[4:11], v[52:59], 0, v243, v243 op_sel_hi:[0,0,0]
	v_mfma_scale_f32_16x16x128_f8f6f4 v[68:71], v[12:19], v[52:59], 0, v243, v243 op_sel_hi:[0,0,0]
	v_mfma_scale_f32_16x16x128_f8f6f4 v[64:67], v[4:11], v[188:195], 0, v243, v243 op_sel_hi:[0,0,0]
	v_mfma_scale_f32_16x16x128_f8f6f4 v[60:63], v[12:19], v[188:195], 0, v243, v243 op_sel_hi:[0,0,0]
	v_mfma_scale_f32_16x16x128_f8f6f4 v[48:51], v[4:11], v[196:203], 0, v243, v243 op_sel_hi:[0,0,0]
	v_mfma_scale_f32_16x16x128_f8f6f4 v[44:47], v[12:19], v[196:203], 0, v243, v243 op_sel_hi:[0,0,0]
	s_setprio 0
	s_setprio 1
	v_mfma_scale_f32_16x16x128_f8f6f4 v[112:115], v[20:27], v[36:43], 0, v243, v243 op_sel_hi:[0,0,0]
	v_mfma_scale_f32_16x16x128_f8f6f4 v[108:111], v[28:35], v[36:43], 0, v243, v243 op_sel_hi:[0,0,0]
	v_mfma_scale_f32_16x16x128_f8f6f4 v[80:83], v[20:27], v[52:59], 0, v243, v243 op_sel_hi:[0,0,0]
	v_mfma_scale_f32_16x16x128_f8f6f4 v[72:75], v[28:35], v[52:59], 0, v243, v243 op_sel_hi:[0,0,0]
	v_mfma_scale_f32_16x16x128_f8f6f4 v[56:59], v[20:27], v[188:195], 0, v243, v243 op_sel_hi:[0,0,0]
	v_mfma_scale_f32_16x16x128_f8f6f4 v[52:55], v[28:35], v[188:195], 0, v243, v243 op_sel_hi:[0,0,0]
	v_mfma_scale_f32_16x16x128_f8f6f4 v[40:43], v[20:27], v[196:203], 0, v243, v243 op_sel_hi:[0,0,0]
	v_mfma_scale_f32_16x16x128_f8f6f4 v[36:39], v[28:35], v[196:203], 0, v243, v243 op_sel_hi:[0,0,0]
	s_setprio 0
	s_barrier
; template <class P, bool ALIGN_EPI>
; __device__ __forceinline__ void gemm_phase(ldsp lds, ldsp tab, const P& S) {
;     ...
;             PG8_TRIP(0, PG8_MMAZ);
;             for (int t = 2; t < nt; t += 2) PG8_TRIP(t, PG8_MMA);
	s_add_i32 s34, 0, 0x18000
	s_add_i32 s46, 0, 0x1c000
	v_add_u32_e32 v188, s34, v185
	v_add_u32_e32 v189, s46, v185
	ds_read_b128 v[28:31], v188
	ds_read_b128 v[32:35], v188 offset:1024
	ds_read_b128 v[20:23], v188 offset:2048
	ds_read_b128 v[24:27], v188 offset:3072
	ds_read_b128 v[12:15], v189
	ds_read_b128 v[16:19], v189 offset:1024
	ds_read_b128 v[4:7], v189 offset:2048
	ds_read_b128 v[8:11], v189 offset:3072
	s_add_u32 s20, s16, 0x70100
	s_addc_u32 s21, s17, 0
	s_mov_b32 m0, s48
	ds_read_b128 v[190:193], v186 offset:32768
	ds_read_b128 v[194:197], v186 offset:33792
	ds_read_b128 v[198:201], v186 offset:34816
	ds_read_b128 v[202:205], v186 offset:35840
	ds_read_b128 v[216:219], v186 offset:36864
	ds_read_b128 v[220:223], v186 offset:37888
	ds_read_b128 v[224:227], v186 offset:38912
	ds_read_b128 v[228:231], v186 offset:39936
	global_load_lds_dwordx4 v2, s[20:21]
	s_mov_b32 m0, s49
	s_nop 0
	global_load_lds_dwordx4 v166, s[20:21]
	s_waitcnt vmcnt(8)
	s_waitcnt lgkmcnt(0)
	s_barrier
	s_setprio 1
	s_waitcnt lgkmcnt(0)
	v_mfma_scale_f32_16x16x128_f8f6f4 v[148:151], v[28:35], v[190:197], v[148:151], v243, v243 op_sel_hi:[0,0,0]
	v_mfma_scale_f32_16x16x128_f8f6f4 v[152:155], v[20:27], v[190:197], v[152:155], v243, v243 op_sel_hi:[0,0,0]
	v_mfma_scale_f32_16x16x128_f8f6f4 v[136:139], v[28:35], v[198:205], v[136:139], v243, v243 op_sel_hi:[0,0,0]
	v_mfma_scale_f32_16x16x128_f8f6f4 v[132:135], v[20:27], v[198:205], v[132:135], v243, v243 op_sel_hi:[0,0,0]
	v_mfma_scale_f32_16x16x128_f8f6f4 v[120:123], v[28:35], v[216:223], v[120:123], v243, v243 op_sel_hi:[0,0,0]
	v_mfma_scale_f32_16x16x128_f8f6f4 v[116:119], v[20:27], v[216:223], v[116:119], v243, v243 op_sel_hi:[0,0,0]
	v_mfma_scale_f32_16x16x128_f8f6f4 v[92:95], v[28:35], v[224:231], v[92:95], v243, v243 op_sel_hi:[0,0,0]
	v_mfma_scale_f32_16x16x128_f8f6f4 v[84:87], v[20:27], v[224:231], v[84:87], v243, v243 op_sel_hi:[0,0,0]
	s_setprio 0
	s_setprio 1
	v_mfma_scale_f32_16x16x128_f8f6f4 v[156:159], v[12:19], v[190:197], v[156:159], v243, v243 op_sel_hi:[0,0,0]
	v_mfma_scale_f32_16x16x128_f8f6f4 v[160:163], v[4:11], v[190:197], v[160:163], v243, v243 op_sel_hi:[0,0,0]
	v_mfma_scale_f32_16x16x128_f8f6f4 v[144:147], v[12:19], v[198:205], v[144:147], v243, v243 op_sel_hi:[0,0,0]
	v_mfma_scale_f32_16x16x128_f8f6f4 v[140:143], v[4:11], v[198:205], v[140:143], v243, v243 op_sel_hi:[0,0,0]
	v_mfma_scale_f32_16x16x128_f8f6f4 v[128:131], v[12:19], v[216:223], v[128:131], v243, v243 op_sel_hi:[0,0,0]
	v_mfma_scale_f32_16x16x128_f8f6f4 v[124:127], v[4:11], v[216:223], v[124:127], v243, v243 op_sel_hi:[0,0,0]
	v_mfma_scale_f32_16x16x128_f8f6f4 v[96:99], v[12:19], v[224:231], v[96:99], v243, v243 op_sel_hi:[0,0,0]
	v_mfma_scale_f32_16x16x128_f8f6f4 v[88:91], v[4:11], v[224:231], v[88:91], v243, v243 op_sel_hi:[0,0,0]
	s_setprio 0
	s_barrier
	s_mov_b64 s[64:65], 0x180
	s_add_i32 s34, s34, s43
	v_lshl_add_u64 v[176:177], v[176:177], 0, s[64:65]
	s_mov_b32 m0, s34
	s_add_i32 s35, s34, 0x2000
	ds_read_b128 v[190:193], v186 offset:49152
	ds_read_b128 v[194:197], v186 offset:50176
	ds_read_b128 v[198:201], v186 offset:51200
	ds_read_b128 v[202:205], v186 offset:52224
	ds_read_b128 v[216:219], v186 offset:53248
	ds_read_b128 v[220:223], v186 offset:54272
	ds_read_b128 v[224:227], v186 offset:55296
	ds_read_b128 v[228:231], v186 offset:56320
	global_load_lds_dwordx4 v[176:177], off
	v_lshl_add_u64 v[176:177], v[178:179], 0, s[64:65]
	s_mov_b32 m0, s35
	s_mov_b64 s[20:21], 0x70180
	global_load_lds_dwordx4 v[176:177], off
	v_lshl_add_u64 v[176:177], v[170:171], 0, s[20:21]
	s_add_i32 s46, s46, s43
	v_readfirstlane_b32 s22, v176
	v_readfirstlane_b32 s23, v177
	s_mov_b32 m0, s46
	s_add_i32 s47, s46, 0x2000
	v_lshl_add_u64 v[176:177], v[180:181], 0, s[64:65]
	s_nop 1
	global_load_lds_dwordx4 v164, s[22:23]
	s_mov_b32 m0, s47
	s_nop 0
	global_load_lds_dwordx4 v168, s[22:23]
	s_mov_b32 m0, s51
	s_nop 0
	global_load_lds_dwordx4 v[176:177], off
	v_lshl_add_u64 v[176:177], v[182:183], 0, s[64:65]
	s_mov_b32 m0, s52
	s_nop 0
	global_load_lds_dwordx4 v[176:177], off
	s_waitcnt vmcnt(8)
	s_waitcnt lgkmcnt(0)
	s_barrier
	s_setprio 1
	s_waitcnt lgkmcnt(0)
	v_mfma_scale_f32_16x16x128_f8f6f4 v[104:107], v[28:35], v[190:197], v[104:107], v243, v243 op_sel_hi:[0,0,0]
	v_mfma_scale_f32_16x16x128_f8f6f4 v[100:103], v[20:27], v[190:197], v[100:103], v243, v243 op_sel_hi:[0,0,0]
	v_mfma_scale_f32_16x16x128_f8f6f4 v[76:79], v[28:35], v[198:205], v[76:79], v243, v243 op_sel_hi:[0,0,0]
	v_mfma_scale_f32_16x16x128_f8f6f4 v[68:71], v[20:27], v[198:205], v[68:71], v243, v243 op_sel_hi:[0,0,0]
	v_mfma_scale_f32_16x16x128_f8f6f4 v[64:67], v[28:35], v[216:223], v[64:67], v243, v243 op_sel_hi:[0,0,0]
	v_mfma_scale_f32_16x16x128_f8f6f4 v[60:63], v[20:27], v[216:223], v[60:63], v243, v243 op_sel_hi:[0,0,0]
	v_mfma_scale_f32_16x16x128_f8f6f4 v[48:51], v[28:35], v[224:231], v[48:51], v243, v243 op_sel_hi:[0,0,0]
	v_mfma_scale_f32_16x16x128_f8f6f4 v[44:47], v[20:27], v[224:231], v[44:47], v243, v243 op_sel_hi:[0,0,0]
	s_setprio 0
	s_setprio 1
	v_mfma_scale_f32_16x16x128_f8f6f4 v[112:115], v[12:19], v[190:197], v[112:115], v243, v243 op_sel_hi:[0,0,0]
	v_mfma_scale_f32_16x16x128_f8f6f4 v[108:111], v[4:11], v[190:197], v[108:111], v243, v243 op_sel_hi:[0,0,0]
	v_mfma_scale_f32_16x16x128_f8f6f4 v[80:83], v[12:19], v[198:205], v[80:83], v243, v243 op_sel_hi:[0,0,0]
	v_mfma_scale_f32_16x16x128_f8f6f4 v[72:75], v[4:11], v[198:205], v[72:75], v243, v243 op_sel_hi:[0,0,0]
	v_mfma_scale_f32_16x16x128_f8f6f4 v[56:59], v[12:19], v[216:223], v[56:59], v243, v243 op_sel_hi:[0,0,0]
	v_mfma_scale_f32_16x16x128_f8f6f4 v[52:55], v[4:11], v[216:223], v[52:55], v243, v243 op_sel_hi:[0,0,0]
	v_mfma_scale_f32_16x16x128_f8f6f4 v[40:43], v[12:19], v[224:231], v[40:43], v243, v243 op_sel_hi:[0,0,0]
	v_mfma_scale_f32_16x16x128_f8f6f4 v[36:39], v[4:11], v[224:231], v[36:39], v243, v243 op_sel_hi:[0,0,0]
	s_setprio 0
	s_barrier
	s_mov_b32 s63, 0
	.p2alignl 6, 3212836864

;     __device__ __forceinline__ bool next(int i, Unit& u) const { return ord.next(i, u); }
; #define PG8_STAGEB(bufoff, gbase) do { _Pragma("unroll") for (int _i = 0; _i < 2; ++_i) PG8_GL((const char*)(gbase) + voffB[_i], bufoff, _i); } while (0)
; #define PG8_STAGEA(bufoff, ubase, offs, h, kb) do { _Pragma("unroll") for (int _i = 0; _i < 2; ++_i) { \
;         if constexpr (P::GATHER) PG8_GL(S.A + (size_t)(kb) + (offs)[h][_i], bufoff, _i); \
;         else PG8_GL((const char*)(ubase) + (size_t)(h) * hstepA + (size_t)(kb) + voffA[_i], bufoff, _i); } } while (0)
;     __device__ __forceinline__ bool next(int i_, Unit& u) const { const bool r = ord.next(i_, u); if (r) mt.locate(u.pm, u.e, u.lt); return r; }
;     __device__ __forceinline__ bool next(int i_, Unit& u) const { const bool r = ord.next(i_, u); if (r) mt.locate(u.pm, u.e, u.lt); return r; }
; template <class P, bool ALIGN_EPI>
; __device__ __forceinline__ void gemm_phase(ldsp lds, ldsp tab, const P& S) {
;     ...
;     Unit cur, nxt; int ui = 0;
;     if (!S.next(0, cur)) return;
;     Acc acc;
;     if constexpr (!P::FP8) {
; #pragma unroll
;         for (int a = 0; a < 2; ++a)
; #pragma unroll
;             for (int b = 0; b < 2; ++b)
; #pragma unroll
;                 for (int m = 0; m < 4; ++m)
; #pragma unroll
;                     for (int n = 0; n < 2; ++n) acc[a][b][m][n] = (f32x4){0.f, 0.f, 0.f, 0.f}; }
;     bf16x8 At[4][2], B0[2][2], B1[2][2];
;     const int sc8 = 0x7F7F7F7F; (void)sc8;
;     const char* cA = S.a_tile(cur); const char* cB = S.b_tile(cur);
;     unsigned goc[2][2] = {{0u, 0u}, {0u, 0u}}, gon[2][2] = {{0u, 0u}, {0u, 0u}};
;     if constexpr (P::GATHER) S.a_offs(cur, goc, sR, sC);
;     S.prepare(cur, 0, tab);
;     PG8_STAGEB(PG8_SB(0, 0), cB); PG8_STAGEB(PG8_SB(0, 1), cB + hstepB); PG8_STAGEA(PG8_SA(0, 0), cA, goc, 0, 0); PG8_STAGEA(PG8_SA(0, 1), cA, goc, 1, 0);
.LBB0_1919:
	s_ashr_i32 s15, s14, 31
	s_lshl_b64 s[16:17], s[14:15], 19
	s_add_u32 s16, s42, s16
	s_addc_u32 s17, s43, s17
	s_ashr_i32 s13, s12, 31
	s_lshl_b64 s[18:19], s[12:13], 19
	s_add_u32 s18, s8, s18
	v_mov_b32_e32 v4, 0
	s_addc_u32 s19, s44, s19
	s_mov_b32 s13, -2
	s_mov_b64 s[30:31], 0x40080
	v_mov_b32_e32 v5, v4
	v_mov_b32_e32 v6, v4
	v_mov_b32_e32 v7, v4
	v_mov_b32_e32 v8, v4
	v_mov_b32_e32 v9, v4
	v_mov_b32_e32 v10, v4
	v_mov_b32_e32 v11, v4
	v_mov_b32_e32 v20, v4
	v_mov_b32_e32 v21, v4
	v_mov_b32_e32 v22, v4
	v_mov_b32_e32 v23, v4
	v_mov_b32_e32 v24, v4
	v_mov_b32_e32 v25, v4
	v_mov_b32_e32 v26, v4
	v_mov_b32_e32 v27, v4
	v_mov_b32_e32 v36, v4
	v_mov_b32_e32 v37, v4
	v_mov_b32_e32 v38, v4
	v_mov_b32_e32 v39, v4
	v_mov_b32_e32 v40, v4
	v_mov_b32_e32 v41, v4
	v_mov_b32_e32 v42, v4
	v_mov_b32_e32 v43, v4
	v_mov_b32_e32 v52, v4
	v_mov_b32_e32 v53, v4
	v_mov_b32_e32 v54, v4
	v_mov_b32_e32 v55, v4
	v_mov_b32_e32 v56, v4
	v_mov_b32_e32 v57, v4
	v_mov_b32_e32 v58, v4
	v_mov_b32_e32 v59, v4
	v_mov_b32_e32 v12, v4
	v_mov_b32_e32 v13, v4
	v_mov_b32_e32 v14, v4
	v_mov_b32_e32 v15, v4
	v_mov_b32_e32 v16, v4
	v_mov_b32_e32 v17, v4
	v_mov_b32_e32 v18, v4
	v_mov_b32_e32 v19, v4
	v_mov_b32_e32 v28, v4
	v_mov_b32_e32 v29, v4
	v_mov_b32_e32 v30, v4
	v_mov_b32_e32 v31, v4
	v_mov_b32_e32 v32, v4
	v_mov_b32_e32 v33, v4
	v_mov_b32_e32 v34, v4
	v_mov_b32_e32 v35, v4
	v_mov_b32_e32 v44, v4
	v_mov_b32_e32 v45, v4
	v_mov_b32_e32 v46, v4
	v_mov_b32_e32 v47, v4
	v_mov_b32_e32 v48, v4
	v_mov_b32_e32 v49, v4
	v_mov_b32_e32 v50, v4
	v_mov_b32_e32 v51, v4
	v_mov_b32_e32 v60, v4
	v_mov_b32_e32 v61, v4
	v_mov_b32_e32 v62, v4
	v_mov_b32_e32 v63, v4
	v_mov_b32_e32 v64, v4
	v_mov_b32_e32 v65, v4
	v_mov_b32_e32 v66, v4
	v_mov_b32_e32 v67, v4
	v_mov_b32_e32 v68, v4
	v_mov_b32_e32 v69, v4
	v_mov_b32_e32 v70, v4
	v_mov_b32_e32 v71, v4
	v_mov_b32_e32 v72, v4
	v_mov_b32_e32 v73, v4
	v_mov_b32_e32 v74, v4
	v_mov_b32_e32 v75, v4
	v_mov_b32_e32 v84, v4
	v_mov_b32_e32 v85, v4
	v_mov_b32_e32 v86, v4
	v_mov_b32_e32 v87, v4
	v_mov_b32_e32 v88, v4
	v_mov_b32_e32 v89, v4
	v_mov_b32_e32 v90, v4
	v_mov_b32_e32 v91, v4
	v_mov_b32_e32 v100, v4
	v_mov_b32_e32 v101, v4
	v_mov_b32_e32 v102, v4
	v_mov_b32_e32 v103, v4
	v_mov_b32_e32 v104, v4
	v_mov_b32_e32 v105, v4
	v_mov_b32_e32 v106, v4
	v_mov_b32_e32 v107, v4
	v_mov_b32_e32 v116, v4
	v_mov_b32_e32 v117, v4
	v_mov_b32_e32 v118, v4
	v_mov_b32_e32 v119, v4
	v_mov_b32_e32 v120, v4
	v_mov_b32_e32 v121, v4
	v_mov_b32_e32 v122, v4
	v_mov_b32_e32 v123, v4
	v_mov_b32_e32 v76, v4
	v_mov_b32_e32 v77, v4
	v_mov_b32_e32 v78, v4
	v_mov_b32_e32 v79, v4
	v_mov_b32_e32 v80, v4
	v_mov_b32_e32 v81, v4
	v_mov_b32_e32 v82, v4
	v_mov_b32_e32 v83, v4
	v_mov_b32_e32 v92, v4
	v_mov_b32_e32 v93, v4
	v_mov_b32_e32 v94, v4
	v_mov_b32_e32 v95, v4
	v_mov_b32_e32 v96, v4
	v_mov_b32_e32 v97, v4
	v_mov_b32_e32 v98, v4
	v_mov_b32_e32 v99, v4
	v_mov_b32_e32 v108, v4
	v_mov_b32_e32 v109, v4
	v_mov_b32_e32 v110, v4
	v_mov_b32_e32 v111, v4
	v_mov_b32_e32 v112, v4
	v_mov_b32_e32 v113, v4
	v_mov_b32_e32 v114, v4
	v_mov_b32_e32 v115, v4
	v_mov_b32_e32 v124, v4
	v_mov_b32_e32 v125, v4
	v_mov_b32_e32 v126, v4
	v_mov_b32_e32 v127, v4
	v_mov_b32_e32 v128, v4
	v_mov_b32_e32 v129, v4
	v_mov_b32_e32 v130, v4
	v_mov_b32_e32 v131, v4
	.p2alignl 6, 3212836864

;     __device__ __forceinline__ bool next(int i, Unit& u) const { return ord.next(i, u); }
; #define PG8_STAGEB(bufoff, gbase) do { _Pragma("unroll") for (int _i = 0; _i < 2; ++_i) PG8_GL((const char*)(gbase) + voffB[_i], bufoff, _i); } while (0)
; #define PG8_STAGEA(bufoff, ubase, offs, h, kb) do { _Pragma("unroll") for (int _i = 0; _i < 2; ++_i) { \
;         if constexpr (P::GATHER) PG8_GL(S.A + (size_t)(kb) + (offs)[h][_i], bufoff, _i); \
;         else PG8_GL((const char*)(ubase) + (size_t)(h) * hstepA + (size_t)(kb) + voffA[_i], bufoff, _i); } } while (0)
;     __device__ __forceinline__ bool next(int i_, Unit& u) const { const bool r = ord.next(i_, u); if (r) mt.locate(u.pm, u.e, u.lt); return r; }
;     __device__ __forceinline__ bool next(int i_, Unit& u) const { const bool r = ord.next(i_, u); if (r) mt.locate(u.pm, u.e, u.lt); return r; }
; template <class P, bool ALIGN_EPI>
; __device__ __forceinline__ void gemm_phase(ldsp lds, ldsp tab, const P& S) {
;     ...
;     Unit cur, nxt; int ui = 0;
;     if (!S.next(0, cur)) return;
;     Acc acc;
;     if constexpr (!P::FP8) {
; #pragma unroll
;         for (int a = 0; a < 2; ++a)
; #pragma unroll
;             for (int b = 0; b < 2; ++b)
; #pragma unroll
;                 for (int m = 0; m < 4; ++m)
; #pragma unroll
;                     for (int n = 0; n < 2; ++n) acc[a][b][m][n] = (f32x4){0.f, 0.f, 0.f, 0.f}; }
;     bf16x8 At[4][2], B0[2][2], B1[2][2];
;     const int sc8 = 0x7F7F7F7F; (void)sc8;
;     const char* cA = S.a_tile(cur); const char* cB = S.b_tile(cur);
;     unsigned goc[2][2] = {{0u, 0u}, {0u, 0u}}, gon[2][2] = {{0u, 0u}, {0u, 0u}};
;     if constexpr (P::GATHER) S.a_offs(cur, goc, sR, sC);
;     S.prepare(cur, 0, tab);
;     PG8_STAGEB(PG8_SB(0, 0), cB); PG8_STAGEB(PG8_SB(0, 1), cB + hstepB); PG8_STAGEA(PG8_SA(0, 0), cA, goc, 0, 0); PG8_STAGEA(PG8_SA(0, 1), cA, goc, 1, 0);
.LBB0_2006:
	v_mov_b32_e32 v4, 0
	s_mov_b32 s2, -2
	s_mov_b64 s[22:23], 0xa0080
	v_mov_b32_e32 v5, v4
	v_mov_b32_e32 v6, v4
	v_mov_b32_e32 v7, v4
	v_mov_b32_e32 v8, v4
	v_mov_b32_e32 v9, v4
	v_mov_b32_e32 v10, v4
	v_mov_b32_e32 v11, v4
	v_mov_b32_e32 v12, v4
	v_mov_b32_e32 v13, v4
	v_mov_b32_e32 v14, v4
	v_mov_b32_e32 v15, v4
	v_mov_b32_e32 v16, v4
	v_mov_b32_e32 v17, v4
	v_mov_b32_e32 v18, v4
	v_mov_b32_e32 v19, v4
	v_mov_b32_e32 v20, v4
	v_mov_b32_e32 v21, v4
	v_mov_b32_e32 v22, v4
	v_mov_b32_e32 v23, v4
	v_mov_b32_e32 v24, v4
	v_mov_b32_e32 v25, v4
	v_mov_b32_e32 v26, v4
	v_mov_b32_e32 v27, v4
	v_mov_b32_e32 v28, v4
	v_mov_b32_e32 v29, v4
	v_mov_b32_e32 v30, v4
	v_mov_b32_e32 v31, v4
	v_mov_b32_e32 v32, v4
	v_mov_b32_e32 v33, v4
	v_mov_b32_e32 v34, v4
	v_mov_b32_e32 v35, v4
	v_mov_b32_e32 v64, v4
	v_mov_b32_e32 v65, v4
	v_mov_b32_e32 v66, v4
	v_mov_b32_e32 v67, v4
	v_mov_b32_e32 v72, v4
	v_mov_b32_e32 v73, v4
	v_mov_b32_e32 v74, v4
	v_mov_b32_e32 v75, v4
	v_mov_b32_e32 v76, v4
	v_mov_b32_e32 v77, v4
	v_mov_b32_e32 v78, v4
	v_mov_b32_e32 v79, v4
	v_mov_b32_e32 v80, v4
	v_mov_b32_e32 v81, v4
	v_mov_b32_e32 v82, v4
	v_mov_b32_e32 v83, v4
	v_mov_b32_e32 v84, v4
	v_mov_b32_e32 v85, v4
	v_mov_b32_e32 v86, v4
	v_mov_b32_e32 v87, v4
	v_mov_b32_e32 v88, v4
	v_mov_b32_e32 v89, v4
	v_mov_b32_e32 v90, v4
	v_mov_b32_e32 v91, v4
	v_mov_b32_e32 v92, v4
	v_mov_b32_e32 v93, v4
	v_mov_b32_e32 v94, v4
	v_mov_b32_e32 v95, v4
	v_mov_b32_e32 v96, v4
	v_mov_b32_e32 v97, v4
	v_mov_b32_e32 v98, v4
	v_mov_b32_e32 v99, v4
	v_mov_b32_e32 v36, v4
	v_mov_b32_e32 v37, v4
	v_mov_b32_e32 v38, v4
	v_mov_b32_e32 v39, v4
	v_mov_b32_e32 v40, v4
	v_mov_b32_e32 v41, v4
	v_mov_b32_e32 v42, v4
	v_mov_b32_e32 v43, v4
	v_mov_b32_e32 v44, v4
	v_mov_b32_e32 v45, v4
	v_mov_b32_e32 v46, v4
	v_mov_b32_e32 v47, v4
	v_mov_b32_e32 v48, v4
	v_mov_b32_e32 v49, v4
	v_mov_b32_e32 v50, v4
	v_mov_b32_e32 v51, v4
	v_mov_b32_e32 v52, v4
	v_mov_b32_e32 v53, v4
	v_mov_b32_e32 v54, v4
	v_mov_b32_e32 v55, v4
	v_mov_b32_e32 v56, v4
	v_mov_b32_e32 v57, v4
	v_mov_b32_e32 v58, v4
	v_mov_b32_e32 v59, v4
	v_mov_b32_e32 v60, v4
	v_mov_b32_e32 v61, v4
	v_mov_b32_e32 v62, v4
	v_mov_b32_e32 v63, v4
	v_mov_b32_e32 v68, v4
	v_mov_b32_e32 v69, v4
	v_mov_b32_e32 v70, v4
	v_mov_b32_e32 v71, v4
	v_mov_b32_e32 v116, v4
	v_mov_b32_e32 v117, v4
	v_mov_b32_e32 v118, v4
	v_mov_b32_e32 v119, v4
	v_mov_b32_e32 v120, v4
	v_mov_b32_e32 v121, v4
	v_mov_b32_e32 v122, v4
	v_mov_b32_e32 v123, v4
	v_mov_b32_e32 v124, v4
	v_mov_b32_e32 v125, v4
	v_mov_b32_e32 v126, v4
	v_mov_b32_e32 v127, v4
	v_mov_b32_e32 v128, v4
	v_mov_b32_e32 v129, v4
	v_mov_b32_e32 v130, v4
	v_mov_b32_e32 v131, v4
	v_mov_b32_e32 v132, v4
	v_mov_b32_e32 v133, v4
	v_mov_b32_e32 v134, v4
	v_mov_b32_e32 v135, v4
	v_mov_b32_e32 v136, v4
	v_mov_b32_e32 v137, v4
	v_mov_b32_e32 v138, v4
	v_mov_b32_e32 v139, v4
	v_mov_b32_e32 v140, v4
	v_mov_b32_e32 v141, v4
	v_mov_b32_e32 v142, v4
	v_mov_b32_e32 v143, v4
	v_mov_b32_e32 v144, v4
	v_mov_b32_e32 v145, v4
	v_mov_b32_e32 v146, v4
	v_mov_b32_e32 v147, v4
	.p2alignl 6, 3212836864
